# combination: cache policies + combine LN-parameter preload + MoE overflow-scan skip + router top-k chains interleaved + p0 weight items in batches of four
# baseline (speedup 1.0000x reference)
.LBB0_1220:
	v_cmp_gt_f32_e64 s[0:1], v27, v20
	v_cmp_gt_f32_e64 s[58:59], v17, v16
	v_cmp_eq_u32_e32 vcc, v152, v22
	s_nop 1
	v_add_u32_e32 v22, 1, v22
	v_cndmask_b32_e64 v190, v16, v17, s[58:59]
	v_cndmask_b32_e64 v23, v20, v27, s[0:1]
	v_cndmask_b32_e64 v191, v152, v156, s[58:59]
	v_cndmask_b32_e64 v24, v152, v156, s[0:1]
	v_cmp_gt_f32_e64 s[58:59], v19, v190
	v_cmp_gt_f32_e64 s[0:1], v25, v23
	s_nop 1
	s_nop 1
	v_cndmask_b32_e64 v190, v190, v19, s[58:59]
	v_cndmask_b32_e64 v23, v23, v25, s[0:1]
	v_cndmask_b32_e64 v191, v191, v157, s[58:59]
	v_cndmask_b32_e64 v24, v24, v157, s[0:1]
	v_cmp_gt_f32_e64 s[58:59], v21, v190
	v_cmp_gt_f32_e64 s[0:1], v15, v23
	s_nop 1
	s_nop 1
	v_cndmask_b32_e64 v190, v190, v21, s[58:59]
	v_cndmask_b32_e64 v23, v23, v15, s[0:1]
	v_max_f32_e32 v193, v190, v190
	v_max_f32_e32 v28, v23, v23
	v_cndmask_b32_e64 v191, v191, v158, s[58:59]
	v_cndmask_b32_e64 v24, v24, v158, s[0:1]
	v_mov_b32_dpp v192, v190 quad_perm:[1,0,3,2] row_mask:0xf bank_mask:0xf bound_ctrl:1
	v_mov_b32_dpp v26, v23 quad_perm:[1,0,3,2] row_mask:0xf bank_mask:0xf bound_ctrl:1
	v_max_f32_e32 v192, v192, v192
	v_max_f32_e32 v26, v26, v26
	v_max_f32_e32 v192, v193, v192
	v_max_f32_e32 v26, v28, v26
	s_nop 1
	s_nop 1
	v_mov_b32_dpp v193, v192 quad_perm:[2,3,0,1] row_mask:0xf bank_mask:0xf bound_ctrl:1
	v_mov_b32_dpp v28, v26 quad_perm:[2,3,0,1] row_mask:0xf bank_mask:0xf bound_ctrl:1
	v_max_f32_e32 v193, v193, v193
	v_max_f32_e32 v28, v28, v28
	v_max_f32_e32 v192, v192, v193
	v_max_f32_e32 v26, v26, v28
	s_nop 1
	s_nop 1
	v_mov_b32_dpp v193, v192 row_half_mirror row_mask:0xf bank_mask:0xf bound_ctrl:1
	v_mov_b32_dpp v28, v26 row_half_mirror row_mask:0xf bank_mask:0xf bound_ctrl:1
	v_max_f32_e32 v193, v193, v193
	v_max_f32_e32 v28, v28, v28
	v_max_f32_e32 v192, v192, v193
	v_max_f32_e32 v26, v26, v28
	s_nop 1
	s_nop 1
	v_mov_b32_dpp v193, v192 row_mirror row_mask:0xf bank_mask:0xf bound_ctrl:1
	v_mov_b32_dpp v28, v26 row_mirror row_mask:0xf bank_mask:0xf bound_ctrl:1
	v_max_f32_e32 v193, v193, v193
	v_max_f32_e32 v28, v28, v28
	v_max_f32_e32 v192, v192, v193
	v_max_f32_e32 v26, v26, v28
	s_nop 0
	s_nop 0
	v_readlane_b32 s56, v192, 32
	v_readlane_b32 s8, v26, 32
	v_readlane_b32 s63, v192, 48
	v_readlane_b32 s9, v26, 48
	v_readlane_b32 s58, v192, 0
	v_readlane_b32 s0, v26, 0
	v_readlane_b32 s59, v192, 16
	v_readlane_b32 s1, v26, 16
	v_max_f32_e64 v192, s63, s63
	v_max_f32_e64 v26, s9, s9
	v_max_f32_e64 v193, s56, s56
	v_max_f32_e64 v28, s8, s8
	v_max_f32_e32 v192, v193, v192
	v_max_f32_e32 v26, v28, v26
	v_mov_b32_e32 v193, s59
	v_mov_b32_e32 v28, s1
	v_max3_f32 v192, s58, v193, v192
	v_max3_f32 v26, s0, v28, v26
	v_cmp_eq_f32_e64 s[58:59], v190, v192
	v_cmp_eq_f32_e64 s[0:1], v23, v26
	s_nop 1
	s_nop 1
	v_cndmask_b32_e64 v190, v230, v191, s[58:59]
	v_cndmask_b32_e64 v23, v230, v24, s[0:1]
	s_nop 1
	s_nop 1
	v_min_i32_dpp v190, v190, v190 quad_perm:[1,0,3,2] row_mask:0xf bank_mask:0xf bound_ctrl:1
	v_min_i32_dpp v23, v23, v23 quad_perm:[1,0,3,2] row_mask:0xf bank_mask:0xf bound_ctrl:1
	s_nop 1
	s_nop 1
	v_min_i32_dpp v190, v190, v190 quad_perm:[2,3,0,1] row_mask:0xf bank_mask:0xf bound_ctrl:1
	v_min_i32_dpp v23, v23, v23 quad_perm:[2,3,0,1] row_mask:0xf bank_mask:0xf bound_ctrl:1
	s_nop 1
	s_nop 1
	v_min_i32_dpp v190, v190, v190 row_half_mirror row_mask:0xf bank_mask:0xf bound_ctrl:1
	v_min_i32_dpp v23, v23, v23 row_half_mirror row_mask:0xf bank_mask:0xf bound_ctrl:1
	s_nop 1
	s_nop 1
	v_min_i32_dpp v190, v190, v190 row_mirror row_mask:0xf bank_mask:0xf bound_ctrl:1
	v_min_i32_dpp v23, v23, v23 row_mirror row_mask:0xf bank_mask:0xf bound_ctrl:1
	s_nop 0
	s_nop 0
	v_readlane_b32 s56, v190, 32
	v_readlane_b32 s8, v23, 32
	v_readlane_b32 s63, v190, 48
	v_readlane_b32 s9, v23, 48
	v_readlane_b32 s59, v190, 16
	v_readlane_b32 s1, v23, 16
	s_min_i32 s56, s56, s63
	s_min_i32 s8, s8, s9
	v_readlane_b32 s58, v190, 0
	v_readlane_b32 s0, v23, 0
	v_mov_b32_e32 v190, s59
	v_mov_b32_e32 v23, s1
	v_mov_b32_e32 v191, s56
	v_mov_b32_e32 v24, s8
	v_min3_i32 v190, s58, v190, v191
	v_min3_i32 v23, s0, v23, v24
	v_cmp_gt_u32_e64 s[58:59], 64, v190
	v_and_b32_e32 v24, 63, v23
	v_readfirstlane_b32 s56, v190
	v_readfirstlane_b32 s8, v23
	s_ashr_i32 s63, s56, 6
	s_ashr_i32 s9, s8, 6
	s_cmp_eq_u32 s63, 1
	s_cselect_b64 s[60:61], -1, 0
	s_cmp_eq_u32 s63, 2
	s_cselect_b64 s[66:67], -1, 0
	s_cmp_eq_u32 s63, 3
	v_cndmask_b32_e64 v192, 0, v11, s[58:59]
	v_cndmask_b32_e64 v193, 0, v12, s[60:61]
	s_cselect_b64 s[68:69], -1, 0
	v_and_b32_e32 v191, 63, v190
	s_cmp_eq_u32 s9, 1
	v_add_f32_e32 v192, v192, v193
	s_cselect_b64 s[46:47], -1, 0
	v_cndmask_b32_e64 v193, 0, v13, s[66:67]
	s_cmp_eq_u32 s9, 2
	v_cndmask_b32_e64 v194, 0, v14, s[68:69]
	v_cmp_gt_u32_e64 s[0:1], 64, v23
	v_add_f32_e32 v193, v193, v194
	s_cselect_b64 s[50:51], -1, 0
	v_cmp_eq_u32_e64 s[70:71], v152, v191
	s_cmp_eq_u32 s9, 3
	v_add_f32_e32 v192, v192, v193
	v_cmp_eq_u32_e64 s[54:55], v152, v24
	v_cndmask_b32_e64 v26, 0, v7, s[0:1]
	v_cndmask_b32_e64 v28, 0, v8, s[46:47]
	s_cselect_b64 s[52:53], -1, 0
	s_and_b64 s[0:1], s[0:1], s[54:55]
	s_and_b64 s[58:59], s[58:59], s[70:71]
	v_add_f32_e32 v26, v26, v28
	v_cndmask_b32_e64 v16, v16, v228, s[58:59]
	v_cndmask_b32_e64 v28, 0, v9, s[50:51]
	s_and_b64 s[58:59], s[70:71], s[60:61]
	v_cndmask_b32_e64 v29, 0, v10, s[52:53]
	v_readlane_b32 s64, v192, s56
	v_cndmask_b32_e64 v20, v20, v228, s[0:1]
	v_cndmask_b32_e64 v17, v17, v228, s[58:59]
	s_and_b64 s[0:1], s[54:55], s[46:47]
	s_and_b64 s[58:59], s[70:71], s[66:67]
	v_add_f32_e32 v28, v28, v29
	v_mov_b32_e32 v191, s64
	v_cndmask_b32_e64 v27, v27, v228, s[0:1]
	v_cndmask_b32_e64 v19, v19, v228, s[58:59]
	s_and_b64 s[0:1], s[54:55], s[50:51]
	s_and_b64 s[58:59], s[70:71], s[68:69]
	v_add_f32_e32 v26, v26, v28
	v_cndmask_b32_e32 v3, v3, v191, vcc
	v_cndmask_b32_e64 v25, v25, v228, s[0:1]
	v_cndmask_b32_e32 v2, v2, v190, vcc
	s_and_b64 s[0:1], s[54:55], s[52:53]
	v_cndmask_b32_e64 v21, v21, v228, s[58:59]
	v_cndmask_b32_e64 v15, v15, v228, s[0:1]
	v_readlane_b32 s65, v26, s8
	v_cndmask_b32_e32 v6, v6, v23, vcc
	s_nop 0
	v_mov_b32_e32 v24, s65
	v_cndmask_b32_e32 v18, v18, v24, vcc
	v_cmp_eq_u32_e32 vcc, 8, v22
	s_nop 0
	v_pk_add_f32 v[4:5], v[4:5], s[64:65]
	s_cbranch_vccz .LBB0_1220
	s_and_saveexec_b64 s[0:1], s[44:45]
	s_mov_b32 s94, 0x3fb8aa3b
	s_mov_b32 s95, 0xc2ce8ed0
	s_mov_b32 s96, 0x42b17218
	s_mov_b64 s[92:93], 0x1fffff
	s_cbranch_execz .LBB0_1050
	v_div_scale_f32 v7, s[8:9], v5, v5, v18
	v_rcp_f32_e32 v9, v7
	s_add_i32 s15, s15, s3
	v_lshl_or_b32 v8, s15, 3, v152
	v_fma_f32 v10, -v7, v9, 1.0
	v_fmac_f32_e32 v9, v10, v9
	v_div_scale_f32 v10, vcc, v18, v5, v18
	v_mul_f32_e32 v11, v10, v9
	v_fma_f32 v12, -v7, v11, v10
	v_fmac_f32_e32 v11, v12, v9
	v_fma_f32 v7, -v7, v11, v10
	v_div_fmas_f32 v7, v7, v9, v11
	v_div_fixup_f32 v5, v7, v5, v18
	v_ashrrev_i32_e32 v9, 31, v8
	v_mul_f32_e32 v5, 0x40200000, v5
	v_lshl_add_u64 v[10:11], v[8:9], 2, s[36:37]
	global_store_dword v[10:11], v5, off
	v_lshlrev_b32_e32 v10, 5, v6
	v_ashrrev_i32_e32 v11, 31, v10
	v_lshl_add_u64 v[10:11], v[10:11], 2, s[16:17]
	global_atomic_add v10, v[10:11], v221, off sc0
	v_ashrrev_i32_e32 v7, 31, v6
	v_lshlrev_b64 v[6:7], 16, v[6:7]
	v_lshl_add_u64 v[6:7], s[48:49], 0, v[6:7]
	v_div_scale_f32 v5, s[8:9], v4, v4, v3
	s_waitcnt vmcnt(0)
	v_ashrrev_i32_e32 v11, 31, v10
	v_lshl_add_u64 v[6:7], v[10:11], 2, v[6:7]
	global_store_dword v[6:7], v8, off
	v_rcp_f32_e32 v7, v5
	v_or_b32_e32 v6, 8, v8
	v_fma_f32 v8, -v5, v7, 1.0
	v_fmac_f32_e32 v7, v8, v7
	v_div_scale_f32 v8, vcc, v3, v4, v3
	v_mul_f32_e32 v9, v8, v7
	v_fma_f32 v10, -v5, v9, v8
	v_fmac_f32_e32 v9, v10, v7
	v_fma_f32 v5, -v5, v9, v8
	v_div_fmas_f32 v5, v5, v7, v9
	v_div_fixup_f32 v3, v5, v4, v3
	v_ashrrev_i32_e32 v7, 31, v6
	v_mul_f32_e32 v3, 0x40200000, v3
	v_lshl_add_u64 v[4:5], v[6:7], 2, s[36:37]
	global_store_dword v[4:5], v3, off
	v_lshlrev_b32_e32 v4, 5, v2
	v_ashrrev_i32_e32 v5, 31, v4
	v_lshl_add_u64 v[4:5], v[4:5], 2, s[16:17]
	global_atomic_add v4, v[4:5], v221, off sc0
	v_ashrrev_i32_e32 v3, 31, v2
	v_lshlrev_b64 v[2:3], 16, v[2:3]
	v_lshl_add_u64 v[2:3], s[48:49], 0, v[2:3]
	s_waitcnt vmcnt(0)
	v_ashrrev_i32_e32 v5, 31, v4
	v_lshl_add_u64 v[2:3], v[4:5], 2, v[2:3]
	global_store_dword v[2:3], v6, off
	s_branch .LBB0_1050
